# dn_intra: hand-scheduled forward substitution (wave 0 inversion), plus radix select
# speedup vs baseline: 1.0085x; 1.0085x over previous
.LBB0_397:
	s_andn2_b64 vcc, exec, s[0:1]
	s_cbranch_vccnz .LBB0_463
	v_and_b32_e32 v10, 32, v107
	v_mul_u32_u24_e32 v2, 0x110, v10
	v_lshlrev_b32_e32 v3, 2, v10
	v_add3_u32 v11, s37, v2, v3
	ds_read_b128 v[124:127], v11 offset:272
	ds_read_b128 v[128:131], v11 offset:544
	ds_read_b128 v[132:135], v11 offset:816
	ds_read_b128 v[136:139], v11 offset:1088
	ds_read_b128 v[140:143], v11 offset:1360
	ds_read_b128 v[144:147], v11 offset:1632
	ds_read_b128 v[148:151], v11 offset:1904
	ds_read_b128 v[152:155], v11 offset:2176
	ds_read_b128 v[156:159], v11 offset:2448
	ds_read_b128 v[160:163], v11 offset:2720
	ds_read_b128 v[164:167], v11 offset:2992
	ds_read_b128 v[168:171], v11 offset:3264
	ds_read_b128 v[172:175], v11 offset:3536
	ds_read_b128 v[176:179], v11 offset:3808
	ds_read_b128 v[184:187], v11 offset:4080
	ds_read_b128 v[188:191], v11 offset:4352
	ds_read_b128 v[200:203], v11 offset:4624
	ds_read_b128 v[204:207], v11 offset:4896
	ds_read_b128 v[208:211], v11 offset:5168
	ds_read_b128 v[212:215], v11 offset:5440
	ds_read_b128 v[216:219], v11 offset:5712
	ds_read_b128 v[220:223], v11 offset:5984
	ds_read_b128 v[224:227], v11 offset:6256
	ds_read_b128 v[228:231], v11 offset:6528
	ds_read_b128 v[232:235], v11 offset:6800
	ds_read_b128 v[236:239], v11 offset:7072
	ds_read_b128 v[240:243], v11 offset:7344
	ds_read_b128 v[244:247], v11 offset:7616
	ds_read_b128 v[248:251], v11 offset:7888
	ds_read_b128 v[4:7], v11 offset:8160
	ds_read_b128 v[12:15], v11 offset:8432
	v_cmp_eq_u32_e64 s[4:5], 0, v109
	v_cmp_eq_u32_e64 s[26:27], 1, v109
	v_cmp_eq_u32_e64 s[80:81], 2, v109
	v_cmp_eq_u32_e64 s[82:83], 3, v109
	v_cndmask_b32_e64 v18, 0, 1.0, s[4:5]
	v_cndmask_b32_e64 v21, 0, 1.0, s[26:27]
	v_cndmask_b32_e64 v23, 0, 1.0, s[80:81]
	v_cndmask_b32_e64 v25, 0, 1.0, s[82:83]
	v_cmp_eq_u32_e64 s[4:5], 4, v109
	v_cmp_eq_u32_e64 s[26:27], 5, v109
	v_cmp_eq_u32_e64 s[80:81], 6, v109
	v_cmp_eq_u32_e64 s[82:83], 7, v109
	v_cndmask_b32_e64 v27, 0, 1.0, s[4:5]
	v_cndmask_b32_e64 v29, 0, 1.0, s[26:27]
	v_cndmask_b32_e64 v31, 0, 1.0, s[80:81]
	v_cndmask_b32_e64 v19, 0, 1.0, s[82:83]
	v_cmp_eq_u32_e64 s[4:5], 8, v109
	v_cmp_eq_u32_e64 s[26:27], 9, v109
	v_cmp_eq_u32_e64 s[80:81], 10, v109
	v_cmp_eq_u32_e64 s[82:83], 11, v109
	v_cndmask_b32_e64 v20, 0, 1.0, s[4:5]
	v_cndmask_b32_e64 v26, 0, 1.0, s[26:27]
	v_cndmask_b32_e64 v22, 0, 1.0, s[80:81]
	v_cndmask_b32_e64 v24, 0, 1.0, s[82:83]
	v_cmp_eq_u32_e64 s[4:5], 12, v109
	v_cmp_eq_u32_e64 s[26:27], 13, v109
	v_cmp_eq_u32_e64 s[80:81], 14, v109
	v_cmp_eq_u32_e64 s[82:83], 15, v109
	v_cndmask_b32_e64 v28, 0, 1.0, s[4:5]
	v_cndmask_b32_e64 v30, 0, 1.0, s[26:27]
	v_cndmask_b32_e64 v32, 0, 1.0, s[80:81]
	v_cndmask_b32_e64 v33, 0, 1.0, s[82:83]
	v_cmp_eq_u32_e64 s[4:5], 16, v109
	v_cmp_eq_u32_e64 s[26:27], 17, v109
	v_cmp_eq_u32_e64 s[80:81], 18, v109
	v_cmp_eq_u32_e64 s[82:83], 19, v109
	v_cndmask_b32_e64 v34, 0, 1.0, s[4:5]
	v_cndmask_b32_e64 v37, 0, 1.0, s[26:27]
	v_cndmask_b32_e64 v35, 0, 1.0, s[80:81]
	v_cndmask_b32_e64 v36, 0, 1.0, s[82:83]
	v_cmp_eq_u32_e64 s[4:5], 20, v109
	v_cmp_eq_u32_e64 s[26:27], 21, v109
	v_cmp_eq_u32_e64 s[80:81], 22, v109
	v_cmp_eq_u32_e64 s[82:83], 23, v109
	v_cndmask_b32_e64 v38, 0, 1.0, s[4:5]
	v_cndmask_b32_e64 v39, 0, 1.0, s[26:27]
	v_cndmask_b32_e64 v40, 0, 1.0, s[80:81]
	v_cndmask_b32_e64 v41, 0, 1.0, s[82:83]
	v_cmp_eq_u32_e64 s[4:5], 24, v109
	v_cmp_eq_u32_e64 s[26:27], 25, v109
	v_cmp_eq_u32_e64 s[80:81], 26, v109
	v_cmp_eq_u32_e64 s[82:83], 27, v109
	v_cndmask_b32_e64 v42, 0, 1.0, s[4:5]
	v_cndmask_b32_e64 v45, 0, 1.0, s[26:27]
	v_cndmask_b32_e64 v43, 0, 1.0, s[80:81]
	v_cndmask_b32_e64 v44, 0, 1.0, s[82:83]
	v_cmp_eq_u32_e64 s[4:5], 28, v109
	v_cmp_eq_u32_e64 s[26:27], 29, v109
	v_cmp_eq_u32_e64 s[80:81], 30, v109
	v_cmp_eq_u32_e64 s[82:83], 31, v109
	v_cndmask_b32_e64 v46, 0, 1.0, s[4:5]
	v_cndmask_b32_e64 v47, 0, 1.0, s[26:27]
	v_cndmask_b32_e64 v48, 0, 1.0, s[80:81]
	v_cndmask_b32_e64 v49, 0, 1.0, s[82:83]
	s_waitcnt lgkmcnt(15)
	v_fma_f32 v21, -v124, v18, v21
	v_fma_f32 v23, -v128, v18, v23
	v_fma_f32 v23, -v129, v21, v23
	v_fma_f32 v25, -v132, v18, v25
	v_fma_f32 v25, -v133, v21, v25
	v_fma_f32 v25, -v134, v23, v25
	v_fma_f32 v27, -v136, v18, v27
	v_fma_f32 v29, -v140, v18, v29
	v_fma_f32 v27, -v137, v21, v27
	v_fma_f32 v29, -v141, v21, v29
	v_fma_f32 v27, -v138, v23, v27
	v_fma_f32 v29, -v142, v23, v29
	v_fma_f32 v27, -v139, v25, v27
	v_fma_f32 v29, -v143, v25, v29
	ds_read_b128 v[140:143], v11 offset:1376
	v_fma_f32 v31, -v144, v18, v31
	v_fma_f32 v19, -v148, v18, v19
	v_fma_f32 v31, -v145, v21, v31
	v_fma_f32 v19, -v149, v21, v19
	v_fma_f32 v31, -v146, v23, v31
	v_fma_f32 v19, -v150, v23, v19
	v_fma_f32 v31, -v147, v25, v31
	v_fma_f32 v19, -v151, v25, v19
	ds_read_b128 v[144:147], v11 offset:1648
	ds_read_b128 v[148:151], v11 offset:1920
	v_fma_f32 v20, -v152, v18, v20
	v_fma_f32 v26, -v156, v18, v26
	v_fma_f32 v20, -v153, v21, v20
	v_fma_f32 v26, -v157, v21, v26
	v_fma_f32 v20, -v154, v23, v20
	v_fma_f32 v26, -v158, v23, v26
	v_fma_f32 v20, -v155, v25, v20
	v_fma_f32 v26, -v159, v25, v26
	ds_read_b128 v[152:155], v11 offset:2192
	ds_read_b128 v[156:159], v11 offset:2464
	v_fma_f32 v22, -v160, v18, v22
	v_fma_f32 v24, -v164, v18, v24
	v_fma_f32 v22, -v161, v21, v22
	v_fma_f32 v24, -v165, v21, v24
	v_fma_f32 v22, -v162, v23, v22
	v_fma_f32 v24, -v166, v23, v24
	v_fma_f32 v22, -v163, v25, v22
	v_fma_f32 v24, -v167, v25, v24
	ds_read_b128 v[160:163], v11 offset:2736
	ds_read_b128 v[164:167], v11 offset:3008
	v_fma_f32 v28, -v168, v18, v28
	v_fma_f32 v30, -v172, v18, v30
	v_fma_f32 v28, -v169, v21, v28
	v_fma_f32 v30, -v173, v21, v30
	v_fma_f32 v28, -v170, v23, v28
	v_fma_f32 v30, -v174, v23, v30
	v_fma_f32 v28, -v171, v25, v28
	v_fma_f32 v30, -v175, v25, v30
	ds_read_b128 v[168:171], v11 offset:3280
	ds_read_b128 v[172:175], v11 offset:3552
	v_fma_f32 v32, -v176, v18, v32
	v_fma_f32 v33, -v184, v18, v33
	v_fma_f32 v32, -v177, v21, v32
	v_fma_f32 v33, -v185, v21, v33
	v_fma_f32 v32, -v178, v23, v32
	v_fma_f32 v33, -v186, v23, v33
	v_fma_f32 v32, -v179, v25, v32
	v_fma_f32 v33, -v187, v25, v33
	ds_read_b128 v[176:179], v11 offset:3824
	ds_read_b128 v[184:187], v11 offset:4096
	s_waitcnt lgkmcnt(15)
	v_fma_f32 v34, -v188, v18, v34
	v_fma_f32 v37, -v200, v18, v37
	v_fma_f32 v34, -v189, v21, v34
	v_fma_f32 v37, -v201, v21, v37
	v_fma_f32 v34, -v190, v23, v34
	v_fma_f32 v37, -v202, v23, v37
	v_fma_f32 v34, -v191, v25, v34
	v_fma_f32 v37, -v203, v25, v37
	ds_read_b128 v[188:191], v11 offset:4368
	ds_read_b128 v[200:203], v11 offset:4640
	v_fma_f32 v35, -v204, v18, v35
	v_fma_f32 v36, -v208, v18, v36
	v_fma_f32 v35, -v205, v21, v35
	v_fma_f32 v36, -v209, v21, v36
	v_fma_f32 v35, -v206, v23, v35
	v_fma_f32 v36, -v210, v23, v36
	v_fma_f32 v35, -v207, v25, v35
	v_fma_f32 v36, -v211, v25, v36
	ds_read_b128 v[204:207], v11 offset:4912
	ds_read_b128 v[208:211], v11 offset:5184
	v_fma_f32 v38, -v212, v18, v38
	v_fma_f32 v39, -v216, v18, v39
	v_fma_f32 v38, -v213, v21, v38
	v_fma_f32 v39, -v217, v21, v39
	v_fma_f32 v38, -v214, v23, v38
	v_fma_f32 v39, -v218, v23, v39
	v_fma_f32 v38, -v215, v25, v38
	v_fma_f32 v39, -v219, v25, v39
	ds_read_b128 v[212:215], v11 offset:5456
	ds_read_b128 v[216:219], v11 offset:5728
	v_fma_f32 v40, -v220, v18, v40
	v_fma_f32 v41, -v224, v18, v41
	v_fma_f32 v40, -v221, v21, v40
	v_fma_f32 v41, -v225, v21, v41
	v_fma_f32 v40, -v222, v23, v40
	v_fma_f32 v41, -v226, v23, v41
	v_fma_f32 v40, -v223, v25, v40
	v_fma_f32 v41, -v227, v25, v41
	ds_read_b128 v[220:223], v11 offset:6000
	ds_read_b128 v[224:227], v11 offset:6272
	v_fma_f32 v42, -v228, v18, v42
	v_fma_f32 v45, -v232, v18, v45
	v_fma_f32 v42, -v229, v21, v42
	v_fma_f32 v45, -v233, v21, v45
	v_fma_f32 v42, -v230, v23, v42
	v_fma_f32 v45, -v234, v23, v45
	v_fma_f32 v42, -v231, v25, v42
	v_fma_f32 v45, -v235, v25, v45
	ds_read_b128 v[228:231], v11 offset:6544
	ds_read_b128 v[232:235], v11 offset:6816
	v_fma_f32 v43, -v236, v18, v43
	v_fma_f32 v44, -v240, v18, v44
	v_fma_f32 v43, -v237, v21, v43
	v_fma_f32 v44, -v241, v21, v44
	v_fma_f32 v43, -v238, v23, v43
	v_fma_f32 v44, -v242, v23, v44
	v_fma_f32 v43, -v239, v25, v43
	v_fma_f32 v44, -v243, v25, v44
	ds_read_b128 v[236:239], v11 offset:7088
	ds_read_b128 v[240:243], v11 offset:7360
	s_waitcnt lgkmcnt(15)
	v_fma_f32 v46, -v244, v18, v46
	v_fma_f32 v47, -v248, v18, v47
	v_fma_f32 v46, -v245, v21, v46
	v_fma_f32 v47, -v249, v21, v47
	v_fma_f32 v46, -v246, v23, v46
	v_fma_f32 v47, -v250, v23, v47
	v_fma_f32 v46, -v247, v25, v46
	v_fma_f32 v47, -v251, v25, v47
	ds_read_b128 v[244:247], v11 offset:7632
	ds_read_b128 v[248:251], v11 offset:7904
	v_fma_f32 v48, -v4, v18, v48
	v_fma_f32 v49, -v12, v18, v49
	v_fma_f32 v48, -v5, v21, v48
	v_fma_f32 v49, -v13, v21, v49
	v_fma_f32 v48, -v6, v23, v48
	v_fma_f32 v49, -v14, v23, v49
	v_fma_f32 v48, -v7, v25, v48
	v_fma_f32 v49, -v15, v25, v49
	ds_read_b128 v[4:7], v11 offset:8176
	ds_read_b128 v[12:15], v11 offset:8448
	v_fma_f32 v29, -v140, v27, v29
	v_fma_f32 v31, -v144, v27, v31
	v_fma_f32 v31, -v145, v29, v31
	v_fma_f32 v19, -v148, v27, v19
	v_fma_f32 v19, -v149, v29, v19
	v_fma_f32 v19, -v150, v31, v19
	v_fma_f32 v20, -v152, v27, v20
	v_fma_f32 v26, -v156, v27, v26
	v_fma_f32 v20, -v153, v29, v20
	v_fma_f32 v26, -v157, v29, v26
	v_fma_f32 v20, -v154, v31, v20
	v_fma_f32 v26, -v158, v31, v26
	v_fma_f32 v20, -v155, v19, v20
	v_fma_f32 v26, -v159, v19, v26
	ds_read_b128 v[156:159], v11 offset:2480
	v_fma_f32 v22, -v160, v27, v22
	v_fma_f32 v24, -v164, v27, v24
	v_fma_f32 v22, -v161, v29, v22
	v_fma_f32 v24, -v165, v29, v24
	v_fma_f32 v22, -v162, v31, v22
	v_fma_f32 v24, -v166, v31, v24
	v_fma_f32 v22, -v163, v19, v22
	v_fma_f32 v24, -v167, v19, v24
	ds_read_b128 v[160:163], v11 offset:2752
	ds_read_b128 v[164:167], v11 offset:3024
	s_waitcnt lgkmcnt(15)
	v_fma_f32 v28, -v168, v27, v28
	v_fma_f32 v30, -v172, v27, v30
	v_fma_f32 v28, -v169, v29, v28
	v_fma_f32 v30, -v173, v29, v30
	v_fma_f32 v28, -v170, v31, v28
	v_fma_f32 v30, -v174, v31, v30
	v_fma_f32 v28, -v171, v19, v28
	v_fma_f32 v30, -v175, v19, v30
	ds_read_b128 v[168:171], v11 offset:3296
	ds_read_b128 v[172:175], v11 offset:3568
	v_fma_f32 v32, -v176, v27, v32
	v_fma_f32 v33, -v184, v27, v33
	v_fma_f32 v32, -v177, v29, v32
	v_fma_f32 v33, -v185, v29, v33
	v_fma_f32 v32, -v178, v31, v32
	v_fma_f32 v33, -v186, v31, v33
	v_fma_f32 v32, -v179, v19, v32
	v_fma_f32 v33, -v187, v19, v33
	ds_read_b128 v[176:179], v11 offset:3840
	ds_read_b128 v[184:187], v11 offset:4112
	v_fma_f32 v34, -v188, v27, v34
	v_fma_f32 v37, -v200, v27, v37
	v_fma_f32 v34, -v189, v29, v34
	v_fma_f32 v37, -v201, v29, v37
	v_fma_f32 v34, -v190, v31, v34
	v_fma_f32 v37, -v202, v31, v37
	v_fma_f32 v34, -v191, v19, v34
	v_fma_f32 v37, -v203, v19, v37
	ds_read_b128 v[188:191], v11 offset:4384
	ds_read_b128 v[200:203], v11 offset:4656
	v_fma_f32 v35, -v204, v27, v35
	v_fma_f32 v36, -v208, v27, v36
	v_fma_f32 v35, -v205, v29, v35
	v_fma_f32 v36, -v209, v29, v36
	v_fma_f32 v35, -v206, v31, v35
	v_fma_f32 v36, -v210, v31, v36
	v_fma_f32 v35, -v207, v19, v35
	v_fma_f32 v36, -v211, v19, v36
	ds_read_b128 v[204:207], v11 offset:4928
	ds_read_b128 v[208:211], v11 offset:5200
	s_waitcnt lgkmcnt(15)
	v_fma_f32 v38, -v212, v27, v38
	v_fma_f32 v39, -v216, v27, v39
	v_fma_f32 v38, -v213, v29, v38
	v_fma_f32 v39, -v217, v29, v39
	v_fma_f32 v38, -v214, v31, v38
	v_fma_f32 v39, -v218, v31, v39
	v_fma_f32 v38, -v215, v19, v38
	v_fma_f32 v39, -v219, v19, v39
	ds_read_b128 v[212:215], v11 offset:5472
	ds_read_b128 v[216:219], v11 offset:5744
	v_fma_f32 v40, -v220, v27, v40
	v_fma_f32 v41, -v224, v27, v41
	v_fma_f32 v40, -v221, v29, v40
	v_fma_f32 v41, -v225, v29, v41
	v_fma_f32 v40, -v222, v31, v40
	v_fma_f32 v41, -v226, v31, v41
	v_fma_f32 v40, -v223, v19, v40
	v_fma_f32 v41, -v227, v19, v41
	ds_read_b128 v[220:223], v11 offset:6016
	ds_read_b128 v[224:227], v11 offset:6288
	v_fma_f32 v42, -v228, v27, v42
	v_fma_f32 v45, -v232, v27, v45
	v_fma_f32 v42, -v229, v29, v42
	v_fma_f32 v45, -v233, v29, v45
	v_fma_f32 v42, -v230, v31, v42
	v_fma_f32 v45, -v234, v31, v45
	v_fma_f32 v42, -v231, v19, v42
	v_fma_f32 v45, -v235, v19, v45
	ds_read_b128 v[228:231], v11 offset:6560
	ds_read_b128 v[232:235], v11 offset:6832
	v_fma_f32 v43, -v236, v27, v43
	v_fma_f32 v44, -v240, v27, v44
	v_fma_f32 v43, -v237, v29, v43
	v_fma_f32 v44, -v241, v29, v44
	v_fma_f32 v43, -v238, v31, v43
	v_fma_f32 v44, -v242, v31, v44
	v_fma_f32 v43, -v239, v19, v43
	v_fma_f32 v44, -v243, v19, v44
	ds_read_b128 v[236:239], v11 offset:7104
	ds_read_b128 v[240:243], v11 offset:7376
	s_waitcnt lgkmcnt(15)
	v_fma_f32 v46, -v244, v27, v46
	v_fma_f32 v47, -v248, v27, v47
	v_fma_f32 v46, -v245, v29, v46
	v_fma_f32 v47, -v249, v29, v47
	v_fma_f32 v46, -v246, v31, v46
	v_fma_f32 v47, -v250, v31, v47
	v_fma_f32 v46, -v247, v19, v46
	v_fma_f32 v47, -v251, v19, v47
	ds_read_b128 v[244:247], v11 offset:7648
	ds_read_b128 v[248:251], v11 offset:7920
	v_fma_f32 v48, -v4, v27, v48
	v_fma_f32 v49, -v12, v27, v49
	v_fma_f32 v48, -v5, v29, v48
	v_fma_f32 v49, -v13, v29, v49
	v_fma_f32 v48, -v6, v31, v48
	v_fma_f32 v49, -v14, v31, v49
	v_fma_f32 v48, -v7, v19, v48
	v_fma_f32 v49, -v15, v19, v49
	ds_read_b128 v[4:7], v11 offset:8192
	ds_read_b128 v[12:15], v11 offset:8464
	v_fma_f32 v26, -v156, v20, v26
	v_fma_f32 v22, -v160, v20, v22
	v_fma_f32 v22, -v161, v26, v22
	v_fma_f32 v24, -v164, v20, v24
	v_fma_f32 v24, -v165, v26, v24
	v_fma_f32 v24, -v166, v22, v24
	s_waitcnt lgkmcnt(15)
	v_fma_f32 v28, -v168, v20, v28
	v_fma_f32 v30, -v172, v20, v30
	v_fma_f32 v28, -v169, v26, v28
	v_fma_f32 v30, -v173, v26, v30
	v_fma_f32 v28, -v170, v22, v28
	v_fma_f32 v30, -v174, v22, v30
	v_fma_f32 v28, -v171, v24, v28
	v_fma_f32 v30, -v175, v24, v30
	ds_read_b128 v[172:175], v11 offset:3584
	v_fma_f32 v32, -v176, v20, v32
	v_fma_f32 v33, -v184, v20, v33
	v_fma_f32 v32, -v177, v26, v32
	v_fma_f32 v33, -v185, v26, v33
	v_fma_f32 v32, -v178, v22, v32
	v_fma_f32 v33, -v186, v22, v33
	v_fma_f32 v32, -v179, v24, v32
	v_fma_f32 v33, -v187, v24, v33
	ds_read_b128 v[176:179], v11 offset:3856
	ds_read_b128 v[184:187], v11 offset:4128
	s_waitcnt lgkmcnt(15)
	v_fma_f32 v34, -v188, v20, v34
	v_fma_f32 v37, -v200, v20, v37
	v_fma_f32 v34, -v189, v26, v34
	v_fma_f32 v37, -v201, v26, v37
	v_fma_f32 v34, -v190, v22, v34
	v_fma_f32 v37, -v202, v22, v37
	v_fma_f32 v34, -v191, v24, v34
	v_fma_f32 v37, -v203, v24, v37
	ds_read_b128 v[188:191], v11 offset:4400
	ds_read_b128 v[200:203], v11 offset:4672
	v_fma_f32 v35, -v204, v20, v35
	v_fma_f32 v36, -v208, v20, v36
	v_fma_f32 v35, -v205, v26, v35
	v_fma_f32 v36, -v209, v26, v36
	v_fma_f32 v35, -v206, v22, v35
	v_fma_f32 v36, -v210, v22, v36
	v_fma_f32 v35, -v207, v24, v35
	v_fma_f32 v36, -v211, v24, v36
	ds_read_b128 v[204:207], v11 offset:4944
	ds_read_b128 v[208:211], v11 offset:5216
	s_waitcnt lgkmcnt(15)
	v_fma_f32 v38, -v212, v20, v38
	v_fma_f32 v39, -v216, v20, v39
	v_fma_f32 v38, -v213, v26, v38
	v_fma_f32 v39, -v217, v26, v39
	v_fma_f32 v38, -v214, v22, v38
	v_fma_f32 v39, -v218, v22, v39
	v_fma_f32 v38, -v215, v24, v38
	v_fma_f32 v39, -v219, v24, v39
	ds_read_b128 v[212:215], v11 offset:5488
	ds_read_b128 v[216:219], v11 offset:5760
	v_fma_f32 v40, -v220, v20, v40
	v_fma_f32 v41, -v224, v20, v41
	v_fma_f32 v40, -v221, v26, v40
	v_fma_f32 v41, -v225, v26, v41
	v_fma_f32 v40, -v222, v22, v40
	v_fma_f32 v41, -v226, v22, v41
	v_fma_f32 v40, -v223, v24, v40
	v_fma_f32 v41, -v227, v24, v41
	ds_read_b128 v[220:223], v11 offset:6032
	ds_read_b128 v[224:227], v11 offset:6304
	s_waitcnt lgkmcnt(15)
	v_fma_f32 v42, -v228, v20, v42
	v_fma_f32 v45, -v232, v20, v45
	v_fma_f32 v42, -v229, v26, v42
	v_fma_f32 v45, -v233, v26, v45
	v_fma_f32 v42, -v230, v22, v42
	v_fma_f32 v45, -v234, v22, v45
	v_fma_f32 v42, -v231, v24, v42
	v_fma_f32 v45, -v235, v24, v45
	ds_read_b128 v[228:231], v11 offset:6576
	ds_read_b128 v[232:235], v11 offset:6848
	v_fma_f32 v43, -v236, v20, v43
	v_fma_f32 v44, -v240, v20, v44
	v_fma_f32 v43, -v237, v26, v43
	v_fma_f32 v44, -v241, v26, v44
	v_fma_f32 v43, -v238, v22, v43
	v_fma_f32 v44, -v242, v22, v44
	v_fma_f32 v43, -v239, v24, v43
	v_fma_f32 v44, -v243, v24, v44
	ds_read_b128 v[236:239], v11 offset:7120
	ds_read_b128 v[240:243], v11 offset:7392
	s_waitcnt lgkmcnt(15)
	v_fma_f32 v46, -v244, v20, v46
	v_fma_f32 v47, -v248, v20, v47
	v_fma_f32 v46, -v245, v26, v46
	v_fma_f32 v47, -v249, v26, v47
	v_fma_f32 v46, -v246, v22, v46
	v_fma_f32 v47, -v250, v22, v47
	v_fma_f32 v46, -v247, v24, v46
	v_fma_f32 v47, -v251, v24, v47
	ds_read_b128 v[244:247], v11 offset:7664
	ds_read_b128 v[248:251], v11 offset:7936
	v_fma_f32 v48, -v4, v20, v48
	v_fma_f32 v49, -v12, v20, v49
	v_fma_f32 v48, -v5, v26, v48
	v_fma_f32 v49, -v13, v26, v49
	v_fma_f32 v48, -v6, v22, v48
	v_fma_f32 v49, -v14, v22, v49
	v_fma_f32 v48, -v7, v24, v48
	v_fma_f32 v49, -v15, v24, v49
	ds_read_b128 v[4:7], v11 offset:8208
	ds_read_b128 v[12:15], v11 offset:8480
	s_waitcnt lgkmcnt(15)
	v_fma_f32 v30, -v172, v28, v30
	v_fma_f32 v32, -v176, v28, v32
	v_fma_f32 v32, -v177, v30, v32
	v_fma_f32 v33, -v184, v28, v33
	v_fma_f32 v33, -v185, v30, v33
	v_fma_f32 v33, -v186, v32, v33
	s_waitcnt lgkmcnt(14)
	v_fma_f32 v34, -v188, v28, v34
	v_fma_f32 v37, -v200, v28, v37
	v_fma_f32 v34, -v189, v30, v34
	v_fma_f32 v37, -v201, v30, v37
	v_fma_f32 v34, -v190, v32, v34
	v_fma_f32 v37, -v202, v32, v37
	v_fma_f32 v34, -v191, v33, v34
	v_fma_f32 v37, -v203, v33, v37
	ds_read_b128 v[200:203], v11 offset:4688
	s_waitcnt lgkmcnt(14)
	s_waitcnt lgkmcnt(13)
	v_fma_f32 v35, -v204, v28, v35
	v_fma_f32 v36, -v208, v28, v36
	v_fma_f32 v35, -v205, v30, v35
	v_fma_f32 v36, -v209, v30, v36
	v_fma_f32 v35, -v206, v32, v35
	v_fma_f32 v36, -v210, v32, v36
	v_fma_f32 v35, -v207, v33, v35
	v_fma_f32 v36, -v211, v33, v36
	ds_read_b128 v[204:207], v11 offset:4960
	ds_read_b128 v[208:211], v11 offset:5232
	s_waitcnt lgkmcnt(14)
	s_waitcnt lgkmcnt(13)
	v_fma_f32 v38, -v212, v28, v38
	v_fma_f32 v39, -v216, v28, v39
	v_fma_f32 v38, -v213, v30, v38
	v_fma_f32 v39, -v217, v30, v39
	v_fma_f32 v38, -v214, v32, v38
	v_fma_f32 v39, -v218, v32, v39
	v_fma_f32 v38, -v215, v33, v38
	v_fma_f32 v39, -v219, v33, v39
	ds_read_b128 v[212:215], v11 offset:5504
	ds_read_b128 v[216:219], v11 offset:5776
	s_waitcnt lgkmcnt(14)
	s_waitcnt lgkmcnt(13)
	v_fma_f32 v40, -v220, v28, v40
	v_fma_f32 v41, -v224, v28, v41
	v_fma_f32 v40, -v221, v30, v40
	v_fma_f32 v41, -v225, v30, v41
	v_fma_f32 v40, -v222, v32, v40
	v_fma_f32 v41, -v226, v32, v41
	v_fma_f32 v40, -v223, v33, v40
	v_fma_f32 v41, -v227, v33, v41
	ds_read_b128 v[220:223], v11 offset:6048
	ds_read_b128 v[224:227], v11 offset:6320
	s_waitcnt lgkmcnt(14)
	s_waitcnt lgkmcnt(13)
	v_fma_f32 v42, -v228, v28, v42
	v_fma_f32 v45, -v232, v28, v45
	v_fma_f32 v42, -v229, v30, v42
	v_fma_f32 v45, -v233, v30, v45
	v_fma_f32 v42, -v230, v32, v42
	v_fma_f32 v45, -v234, v32, v45
	v_fma_f32 v42, -v231, v33, v42
	v_fma_f32 v45, -v235, v33, v45
	ds_read_b128 v[228:231], v11 offset:6592
	ds_read_b128 v[232:235], v11 offset:6864
	s_waitcnt lgkmcnt(14)
	s_waitcnt lgkmcnt(13)
	v_fma_f32 v43, -v236, v28, v43
	v_fma_f32 v44, -v240, v28, v44
	v_fma_f32 v43, -v237, v30, v43
	v_fma_f32 v44, -v241, v30, v44
	v_fma_f32 v43, -v238, v32, v43
	v_fma_f32 v44, -v242, v32, v44
	v_fma_f32 v43, -v239, v33, v43
	v_fma_f32 v44, -v243, v33, v44
	ds_read_b128 v[236:239], v11 offset:7136
	ds_read_b128 v[240:243], v11 offset:7408
	s_waitcnt lgkmcnt(14)
	s_waitcnt lgkmcnt(13)
	v_fma_f32 v46, -v244, v28, v46
	v_fma_f32 v47, -v248, v28, v47
	v_fma_f32 v46, -v245, v30, v46
	v_fma_f32 v47, -v249, v30, v47
	v_fma_f32 v46, -v246, v32, v46
	v_fma_f32 v47, -v250, v32, v47
	v_fma_f32 v46, -v247, v33, v46
	v_fma_f32 v47, -v251, v33, v47
	ds_read_b128 v[244:247], v11 offset:7680
	ds_read_b128 v[248:251], v11 offset:7952
	s_waitcnt lgkmcnt(14)
	s_waitcnt lgkmcnt(13)
	v_fma_f32 v48, -v4, v28, v48
	v_fma_f32 v49, -v12, v28, v49
	v_fma_f32 v48, -v5, v30, v48
	v_fma_f32 v49, -v13, v30, v49
	v_fma_f32 v48, -v6, v32, v48
	v_fma_f32 v49, -v14, v32, v49
	v_fma_f32 v48, -v7, v33, v48
	v_fma_f32 v49, -v15, v33, v49
	ds_read_b128 v[4:7], v11 offset:8224
	ds_read_b128 v[12:15], v11 offset:8496
	s_waitcnt lgkmcnt(14)
	v_fma_f32 v37, -v200, v34, v37
	s_waitcnt lgkmcnt(13)
	v_fma_f32 v35, -v204, v34, v35
	v_fma_f32 v35, -v205, v37, v35
	s_waitcnt lgkmcnt(12)
	v_fma_f32 v36, -v208, v34, v36
	v_fma_f32 v36, -v209, v37, v36
	v_fma_f32 v36, -v210, v35, v36
	s_waitcnt lgkmcnt(11)
	s_waitcnt lgkmcnt(10)
	v_fma_f32 v38, -v212, v34, v38
	v_fma_f32 v39, -v216, v34, v39
	v_fma_f32 v38, -v213, v37, v38
	v_fma_f32 v39, -v217, v37, v39
	v_fma_f32 v38, -v214, v35, v38
	v_fma_f32 v39, -v218, v35, v39
	v_fma_f32 v38, -v215, v36, v38
	v_fma_f32 v39, -v219, v36, v39
	ds_read_b128 v[216:219], v11 offset:5792
	s_waitcnt lgkmcnt(10)
	s_waitcnt lgkmcnt(9)
	v_fma_f32 v40, -v220, v34, v40
	v_fma_f32 v41, -v224, v34, v41
	v_fma_f32 v40, -v221, v37, v40
	v_fma_f32 v41, -v225, v37, v41
	v_fma_f32 v40, -v222, v35, v40
	v_fma_f32 v41, -v226, v35, v41
	v_fma_f32 v40, -v223, v36, v40
	v_fma_f32 v41, -v227, v36, v41
	ds_read_b128 v[220:223], v11 offset:6064
	ds_read_b128 v[224:227], v11 offset:6336
	s_waitcnt lgkmcnt(10)
	s_waitcnt lgkmcnt(9)
	v_fma_f32 v42, -v228, v34, v42
	v_fma_f32 v45, -v232, v34, v45
	v_fma_f32 v42, -v229, v37, v42
	v_fma_f32 v45, -v233, v37, v45
	v_fma_f32 v42, -v230, v35, v42
	v_fma_f32 v45, -v234, v35, v45
	v_fma_f32 v42, -v231, v36, v42
	v_fma_f32 v45, -v235, v36, v45
	ds_read_b128 v[228:231], v11 offset:6608
	ds_read_b128 v[232:235], v11 offset:6880
	s_waitcnt lgkmcnt(10)
	s_waitcnt lgkmcnt(9)
	v_fma_f32 v43, -v236, v34, v43
	v_fma_f32 v44, -v240, v34, v44
	v_fma_f32 v43, -v237, v37, v43
	v_fma_f32 v44, -v241, v37, v44
	v_fma_f32 v43, -v238, v35, v43
	v_fma_f32 v44, -v242, v35, v44
	v_fma_f32 v43, -v239, v36, v43
	v_fma_f32 v44, -v243, v36, v44
	ds_read_b128 v[236:239], v11 offset:7152
	ds_read_b128 v[240:243], v11 offset:7424
	s_waitcnt lgkmcnt(10)
	s_waitcnt lgkmcnt(9)
	v_fma_f32 v46, -v244, v34, v46
	v_fma_f32 v47, -v248, v34, v47
	v_fma_f32 v46, -v245, v37, v46
	v_fma_f32 v47, -v249, v37, v47
	v_fma_f32 v46, -v246, v35, v46
	v_fma_f32 v47, -v250, v35, v47
	v_fma_f32 v46, -v247, v36, v46
	v_fma_f32 v47, -v251, v36, v47
	ds_read_b128 v[244:247], v11 offset:7696
	ds_read_b128 v[248:251], v11 offset:7968
	s_waitcnt lgkmcnt(10)
	s_waitcnt lgkmcnt(9)
	v_fma_f32 v48, -v4, v34, v48
	v_fma_f32 v49, -v12, v34, v49
	v_fma_f32 v48, -v5, v37, v48
	v_fma_f32 v49, -v13, v37, v49
	v_fma_f32 v48, -v6, v35, v48
	v_fma_f32 v49, -v14, v35, v49
	v_fma_f32 v48, -v7, v36, v48
	v_fma_f32 v49, -v15, v36, v49
	ds_read_b128 v[4:7], v11 offset:8240
	ds_read_b128 v[12:15], v11 offset:8512
	s_waitcnt lgkmcnt(10)
	v_fma_f32 v39, -v216, v38, v39
	s_waitcnt lgkmcnt(9)
	v_fma_f32 v40, -v220, v38, v40
	v_fma_f32 v40, -v221, v39, v40
	s_waitcnt lgkmcnt(8)
	v_fma_f32 v41, -v224, v38, v41
	v_fma_f32 v41, -v225, v39, v41
	v_fma_f32 v41, -v226, v40, v41
	s_waitcnt lgkmcnt(7)
	s_waitcnt lgkmcnt(6)
	v_fma_f32 v42, -v228, v38, v42
	v_fma_f32 v45, -v232, v38, v45
	v_fma_f32 v42, -v229, v39, v42
	v_fma_f32 v45, -v233, v39, v45
	v_fma_f32 v42, -v230, v40, v42
	v_fma_f32 v45, -v234, v40, v45
	v_fma_f32 v42, -v231, v41, v42
	v_fma_f32 v45, -v235, v41, v45
	ds_read_b128 v[232:235], v11 offset:6896
	s_waitcnt lgkmcnt(6)
	s_waitcnt lgkmcnt(5)
	v_fma_f32 v43, -v236, v38, v43
	v_fma_f32 v44, -v240, v38, v44
	v_fma_f32 v43, -v237, v39, v43
	v_fma_f32 v44, -v241, v39, v44
	v_fma_f32 v43, -v238, v40, v43
	v_fma_f32 v44, -v242, v40, v44
	v_fma_f32 v43, -v239, v41, v43
	v_fma_f32 v44, -v243, v41, v44
	ds_read_b128 v[236:239], v11 offset:7168
	ds_read_b128 v[240:243], v11 offset:7440
	s_waitcnt lgkmcnt(6)
	s_waitcnt lgkmcnt(5)
	v_fma_f32 v46, -v244, v38, v46
	v_fma_f32 v47, -v248, v38, v47
	v_fma_f32 v46, -v245, v39, v46
	v_fma_f32 v47, -v249, v39, v47
	v_fma_f32 v46, -v246, v40, v46
	v_fma_f32 v47, -v250, v40, v47
	v_fma_f32 v46, -v247, v41, v46
	v_fma_f32 v47, -v251, v41, v47
	ds_read_b128 v[244:247], v11 offset:7712
	ds_read_b128 v[248:251], v11 offset:7984
	s_waitcnt lgkmcnt(6)
	s_waitcnt lgkmcnt(5)
	v_fma_f32 v48, -v4, v38, v48
	v_fma_f32 v49, -v12, v38, v49
	v_fma_f32 v48, -v5, v39, v48
	v_fma_f32 v49, -v13, v39, v49
	v_fma_f32 v48, -v6, v40, v48
	v_fma_f32 v49, -v14, v40, v49
	v_fma_f32 v48, -v7, v41, v48
	v_fma_f32 v49, -v15, v41, v49
	ds_read_b128 v[4:7], v11 offset:8256
	ds_read_b128 v[12:15], v11 offset:8528
	s_waitcnt lgkmcnt(6)
	v_fma_f32 v45, -v232, v42, v45
	s_waitcnt lgkmcnt(5)
	v_fma_f32 v43, -v236, v42, v43
	v_fma_f32 v43, -v237, v45, v43
	s_waitcnt lgkmcnt(4)
	v_fma_f32 v44, -v240, v42, v44
	v_fma_f32 v44, -v241, v45, v44
	v_fma_f32 v44, -v242, v43, v44
	s_waitcnt lgkmcnt(3)
	s_waitcnt lgkmcnt(2)
	v_fma_f32 v46, -v244, v42, v46
	v_fma_f32 v47, -v248, v42, v47
	v_fma_f32 v46, -v245, v45, v46
	v_fma_f32 v47, -v249, v45, v47
	v_fma_f32 v46, -v246, v43, v46
	v_fma_f32 v47, -v250, v43, v47
	v_fma_f32 v46, -v247, v44, v46
	v_fma_f32 v47, -v251, v44, v47
	ds_read_b128 v[248:251], v11 offset:8000
	s_waitcnt lgkmcnt(2)
	s_waitcnt lgkmcnt(1)
	v_fma_f32 v48, -v4, v42, v48
	v_fma_f32 v49, -v12, v42, v49
	v_fma_f32 v48, -v5, v45, v48
	v_fma_f32 v49, -v13, v45, v49
	v_fma_f32 v48, -v6, v43, v48
	v_fma_f32 v49, -v14, v43, v49
	v_fma_f32 v48, -v7, v44, v48
	v_fma_f32 v49, -v15, v44, v49
	ds_read_b128 v[4:7], v11 offset:8272
	ds_read_b128 v[12:15], v11 offset:8544
	s_waitcnt lgkmcnt(2)
	v_fma_f32 v47, -v248, v46, v47
	s_waitcnt lgkmcnt(1)
	v_fma_f32 v48, -v4, v46, v48
	v_fma_f32 v48, -v5, v47, v48
	s_waitcnt lgkmcnt(0)
	v_fma_f32 v49, -v12, v46, v49
	v_fma_f32 v49, -v13, v47, v49
	v_fma_f32 v49, -v14, v48, v49
	v_lshlrev_b32_e32 v2, 1, v107
	v_and_b32_e32 v2, 0x7e, v2
	v_add_u32_e32 v3, s72, v2
	v_lshlrev_b32_e32 v50, 1, v109
	v_cvt_pk_bf16_f32 v2, v18, s0
	v_mad_u32_u24 v4, v10, s73, v3
	v_cmp_gt_u32_e32 vcc, 32, v100
	ds_write_b16 v4, v2
	v_add_u32_e32 v2, s72, v50
	s_and_saveexec_b64 s[0:1], vcc
	ds_write_b16 v2, v99 offset:64
	s_or_b64 exec, exec, s[0:1]
	v_mul_u32_u24_e32 v51, 0x90, v10
	v_cvt_pk_bf16_f32 v4, v21, s0
	v_add_u32_e32 v3, v3, v51
	ds_write_b16 v3, v4 offset:144
	s_and_saveexec_b64 s[0:1], vcc
	ds_write_b16 v2, v99 offset:208
	s_or_b64 exec, exec, s[0:1]
	v_cvt_pk_bf16_f32 v4, v23, s0
	ds_write_b16 v3, v4 offset:288
	s_and_saveexec_b64 s[0:1], vcc
	ds_write_b16 v2, v99 offset:352
	s_or_b64 exec, exec, s[0:1]
	v_cvt_pk_bf16_f32 v4, v25, s0
	ds_write_b16 v3, v4 offset:432
	s_and_saveexec_b64 s[0:1], vcc
	ds_write_b16 v2, v99 offset:496
	s_or_b64 exec, exec, s[0:1]
	v_cvt_pk_bf16_f32 v4, v27, s0
	ds_write_b16 v3, v4 offset:576
	s_and_saveexec_b64 s[0:1], vcc
	ds_write_b16 v2, v99 offset:640
	s_or_b64 exec, exec, s[0:1]
	v_cvt_pk_bf16_f32 v4, v29, s0
	ds_write_b16 v3, v4 offset:720
	s_and_saveexec_b64 s[0:1], vcc
	ds_write_b16 v2, v99 offset:784
	s_or_b64 exec, exec, s[0:1]
	v_cvt_pk_bf16_f32 v4, v31, s0
	ds_write_b16 v3, v4 offset:864
	s_and_saveexec_b64 s[0:1], vcc
	ds_write_b16 v2, v99 offset:928
	s_or_b64 exec, exec, s[0:1]
	v_cvt_pk_bf16_f32 v4, v19, s0
	ds_write_b16 v3, v4 offset:1008
	s_and_saveexec_b64 s[0:1], vcc
	ds_write_b16 v2, v99 offset:1072
	s_or_b64 exec, exec, s[0:1]
	v_cvt_pk_bf16_f32 v4, v20, s0
	ds_write_b16 v3, v4 offset:1152
	s_and_saveexec_b64 s[0:1], vcc
	ds_write_b16 v2, v99 offset:1216
	s_or_b64 exec, exec, s[0:1]
	v_cvt_pk_bf16_f32 v4, v26, s0
	ds_write_b16 v3, v4 offset:1296
	s_and_saveexec_b64 s[0:1], vcc
	ds_write_b16 v2, v99 offset:1360
	s_or_b64 exec, exec, s[0:1]
	v_cvt_pk_bf16_f32 v4, v22, s0
	ds_write_b16 v3, v4 offset:1440
	s_and_saveexec_b64 s[0:1], vcc
	ds_write_b16 v2, v99 offset:1504
	s_or_b64 exec, exec, s[0:1]
	v_cvt_pk_bf16_f32 v4, v24, s0
	ds_write_b16 v3, v4 offset:1584
	s_and_saveexec_b64 s[0:1], vcc
	ds_write_b16 v2, v99 offset:1648
	s_or_b64 exec, exec, s[0:1]
	v_cvt_pk_bf16_f32 v4, v28, s0
	ds_write_b16 v3, v4 offset:1728
	s_and_saveexec_b64 s[0:1], vcc
	ds_write_b16 v2, v99 offset:1792
	s_or_b64 exec, exec, s[0:1]
	v_cvt_pk_bf16_f32 v4, v30, s0
	ds_write_b16 v3, v4 offset:1872
	s_and_saveexec_b64 s[0:1], vcc
	ds_write_b16 v2, v99 offset:1936
	s_or_b64 exec, exec, s[0:1]
	v_cvt_pk_bf16_f32 v4, v32, s0
	ds_write_b16 v3, v4 offset:2016
	s_and_saveexec_b64 s[0:1], vcc
	ds_write_b16 v2, v99 offset:2080
	s_or_b64 exec, exec, s[0:1]
	v_cvt_pk_bf16_f32 v4, v33, s0
	ds_write_b16 v3, v4 offset:2160
	s_and_saveexec_b64 s[0:1], vcc
	ds_write_b16 v2, v99 offset:2224
	s_or_b64 exec, exec, s[0:1]
	v_cvt_pk_bf16_f32 v4, v34, s0
	ds_write_b16 v3, v4 offset:2304
	s_and_saveexec_b64 s[0:1], vcc
	ds_write_b16 v2, v99 offset:2368
	s_or_b64 exec, exec, s[0:1]
	v_cvt_pk_bf16_f32 v4, v37, s0
	ds_write_b16 v3, v4 offset:2448
	s_and_saveexec_b64 s[0:1], vcc
	ds_write_b16 v2, v99 offset:2512
	s_or_b64 exec, exec, s[0:1]
	v_cvt_pk_bf16_f32 v4, v35, s0
	ds_write_b16 v3, v4 offset:2592
	s_and_saveexec_b64 s[0:1], vcc
	ds_write_b16 v2, v99 offset:2656
	s_or_b64 exec, exec, s[0:1]
	v_cvt_pk_bf16_f32 v4, v36, s0
	ds_write_b16 v3, v4 offset:2736
	s_and_saveexec_b64 s[0:1], vcc
	ds_write_b16 v2, v99 offset:2800
	s_or_b64 exec, exec, s[0:1]
	v_cvt_pk_bf16_f32 v4, v38, s0
	ds_write_b16 v3, v4 offset:2880
	s_and_saveexec_b64 s[0:1], vcc
	ds_write_b16 v2, v99 offset:2944
	s_or_b64 exec, exec, s[0:1]
	v_cvt_pk_bf16_f32 v4, v39, s0
	ds_write_b16 v3, v4 offset:3024
	s_and_saveexec_b64 s[0:1], vcc
	ds_write_b16 v2, v99 offset:3088
	s_or_b64 exec, exec, s[0:1]
	v_cvt_pk_bf16_f32 v4, v40, s0
	ds_write_b16 v3, v4 offset:3168
	s_and_saveexec_b64 s[0:1], vcc
	ds_write_b16 v2, v99 offset:3232
	s_or_b64 exec, exec, s[0:1]
	v_cvt_pk_bf16_f32 v4, v41, s0
	ds_write_b16 v3, v4 offset:3312
	s_and_saveexec_b64 s[0:1], vcc
	ds_write_b16 v2, v99 offset:3376
	s_or_b64 exec, exec, s[0:1]
	v_cvt_pk_bf16_f32 v4, v42, s0
	ds_write_b16 v3, v4 offset:3456
	s_and_saveexec_b64 s[0:1], vcc
	ds_write_b16 v2, v99 offset:3520
	s_or_b64 exec, exec, s[0:1]
	v_cvt_pk_bf16_f32 v4, v45, s0
	ds_write_b16 v3, v4 offset:3600
	s_and_saveexec_b64 s[0:1], vcc
	ds_write_b16 v2, v99 offset:3664
	s_or_b64 exec, exec, s[0:1]
	v_cvt_pk_bf16_f32 v4, v43, s0
	ds_write_b16 v3, v4 offset:3744
	s_and_saveexec_b64 s[0:1], vcc
	ds_write_b16 v2, v99 offset:3808
	s_or_b64 exec, exec, s[0:1]
	v_cvt_pk_bf16_f32 v4, v44, s0
	ds_write_b16 v3, v4 offset:3888
	s_and_saveexec_b64 s[0:1], vcc
	ds_write_b16 v2, v99 offset:3952
	s_or_b64 exec, exec, s[0:1]
	v_cvt_pk_bf16_f32 v4, v46, s0
	ds_write_b16 v3, v4 offset:4032
	s_and_saveexec_b64 s[0:1], vcc
	ds_write_b16 v2, v99 offset:4096
	s_or_b64 exec, exec, s[0:1]
	v_cvt_pk_bf16_f32 v4, v47, s0
	ds_write_b16 v3, v4 offset:4176
	s_and_saveexec_b64 s[0:1], vcc
	ds_write_b16 v2, v99 offset:4240
	s_or_b64 exec, exec, s[0:1]
	v_cvt_pk_bf16_f32 v4, v48, s0
	ds_write_b16 v3, v4 offset:4320
	s_and_saveexec_b64 s[0:1], vcc
	ds_write_b16 v2, v99 offset:4384
	s_or_b64 exec, exec, s[0:1]
	v_cvt_pk_bf16_f32 v4, v49, s0
	ds_write_b16 v3, v4 offset:4464
	s_and_saveexec_b64 s[0:1], vcc
	ds_write_b16 v2, v99 offset:4528
	s_or_b64 exec, exec, s[0:1]
	v_and_b32_e32 v2, 16, v107
	v_lshlrev_b32_e32 v3, 2, v107
	v_and_or_b32 v2, v3, 12, v2
	v_lshlrev_b32_e32 v60, 3, v110
	v_lshlrev_b32_e32 v10, 1, v2
	v_mov_b32_e32 v2, s41
	v_mad_u32_u24 v54, v109, s42, v2
	v_or_b32_e32 v2, v60, v112
	s_waitcnt lgkmcnt(0)
	v_mul_u32_u24_e32 v6, 0x90, v2
	v_lshl_add_u32 v2, v110, 4, v54
	ds_read_b128 v[2:5], v2
	v_add3_u32 v8, s72, v6, v10
	ds_read_b64_tr_b16 v[6:7], v8
	ds_read_b64_tr_b16 v[8:9], v8 offset:576
	v_or_b32_e32 v55, 16, v60
	v_or_b32_e32 v11, v55, v112
	v_mul_u32_u24_e32 v11, 0x90, v11
	v_add3_u32 v61, s72, v11, v10
	s_waitcnt lgkmcnt(0)
	v_mfma_f32_32x32x16_bf16 v[2:17], v[2:5], v[6:9], 0
	v_lshl_add_u32 v54, v55, 1, v54
	ds_read_b64_tr_b16 v[52:53], v61
	ds_read_b128 v[56:59], v54
	ds_read_b64_tr_b16 v[54:55], v61 offset:576
	v_mul_u32_u24_e32 v61, 0x90, v109
	v_add3_u32 v60, s72, v61, v60
	s_waitcnt lgkmcnt(0)
	v_mfma_f32_32x32x16_bf16 v[2:17], v[56:59], v[52:55], v[2:17]
	v_add_u32_e32 v52, 0x1000, v60
	s_nop 10
	v_cvt_pk_bf16_f32 v2, v2, v3
	v_cvt_pk_bf16_f32 v3, v4, v5
	v_cvt_pk_bf16_f32 v4, v6, v7
	v_cvt_pk_bf16_f32 v5, v8, v9
	ds_read2_b64 v[6:9], v52 offset0:72 offset1:74
	ds_read2_b64 v[52:55], v52 offset0:76 offset1:78
	v_cvt_pk_bf16_f32 v56, v10, v11
	s_waitcnt lgkmcnt(0)
	v_lshl_add_u32 v10, v100, 2, s79
	ds_read_b32 v60, v10
	v_lshl_add_u32 v10, v109, 2, s79
	ds_read_b32 v61, v10
	v_lshlrev_b32_e32 v10, 1, v100
	v_cvt_pk_bf16_f32 v57, v12, v13
	s_waitcnt lgkmcnt(1)
	v_mul_f32_e32 v11, v18, v60
	v_add3_u32 v18, s72, v10, v51
	v_mul_f32_e32 v10, v21, v60
	v_cvt_pk_bf16_f32 v10, v10, s0
	ds_write_b16 v18, v10 offset:144
	v_mul_f32_e32 v10, v23, v60
	v_cvt_pk_bf16_f32 v10, v10, s0
	ds_write_b16 v18, v10 offset:288
	v_mul_f32_e32 v10, v25, v60
	v_cvt_pk_bf16_f32 v10, v10, s0
	ds_write_b16 v18, v10 offset:432
	v_mul_f32_e32 v10, v27, v60
	v_cvt_pk_bf16_f32 v10, v10, s0
	ds_write_b16 v18, v10 offset:576
	v_mul_f32_e32 v10, v29, v60
	v_cvt_pk_bf16_f32 v10, v10, s0
	ds_write_b16 v18, v10 offset:720
	v_mul_f32_e32 v10, v31, v60
	v_cvt_pk_bf16_f32 v10, v10, s0
	ds_write_b16 v18, v10 offset:864
	v_mul_f32_e32 v10, v19, v60
	v_cvt_pk_bf16_f32 v10, v10, s0
	ds_write_b16 v18, v10 offset:1008
	v_mul_f32_e32 v10, v20, v60
	v_cvt_pk_bf16_f32 v10, v10, s0
	ds_write_b16 v18, v10 offset:1152
	v_mul_f32_e32 v10, v26, v60
	v_cvt_pk_bf16_f32 v10, v10, s0
	ds_write_b16 v18, v10 offset:1296
	v_mul_f32_e32 v10, v22, v60
	v_cvt_pk_bf16_f32 v10, v10, s0
	ds_write_b16 v18, v10 offset:1440
	v_mul_f32_e32 v10, v24, v60
	v_cvt_pk_bf16_f32 v10, v10, s0
	ds_write_b16 v18, v10 offset:1584
	v_mul_f32_e32 v10, v28, v60
	v_cvt_pk_bf16_f32 v10, v10, s0
	ds_write_b16 v18, v10 offset:1728
	v_mul_f32_e32 v10, v30, v60
	v_cvt_pk_bf16_f32 v10, v10, s0
	ds_write_b16 v18, v10 offset:1872
	v_mul_f32_e32 v10, v32, v60
	v_cvt_pk_bf16_f32 v10, v10, s0
	ds_write_b16 v18, v10 offset:2016
	v_mul_f32_e32 v10, v33, v60
	v_cvt_pk_bf16_f32 v10, v10, s0
	ds_write_b16 v18, v10 offset:2160
	v_mul_f32_e32 v10, v34, v60
	v_cvt_pk_bf16_f32 v10, v10, s0
	ds_write_b16 v18, v10 offset:2304
	v_mul_f32_e32 v10, v37, v60
	v_cvt_pk_bf16_f32 v10, v10, s0
	ds_write_b16 v18, v10 offset:2448
	v_mul_f32_e32 v10, v35, v60
	v_cvt_pk_bf16_f32 v10, v10, s0
	ds_write_b16 v18, v10 offset:2592
	v_mul_f32_e32 v10, v36, v60
	v_cvt_pk_bf16_f32 v10, v10, s0
	ds_write_b16 v18, v10 offset:2736
	v_mul_f32_e32 v10, v38, v60
	v_cvt_pk_bf16_f32 v10, v10, s0
	ds_write_b16 v18, v10 offset:2880
	v_mul_f32_e32 v10, v39, v60
	v_cvt_pk_bf16_f32 v10, v10, s0
	ds_write_b16 v18, v10 offset:3024
	v_mul_f32_e32 v10, v40, v60
	v_cvt_pk_bf16_f32 v10, v10, s0
	ds_write_b16 v18, v10 offset:3168
	v_mul_f32_e32 v10, v41, v60
	v_cvt_pk_bf16_f32 v10, v10, s0
	ds_write_b16 v18, v10 offset:3312
	v_mul_f32_e32 v10, v42, v60
	v_cvt_pk_bf16_f32 v10, v10, s0
	ds_write_b16 v18, v10 offset:3456
	v_mul_f32_e32 v10, v45, v60
	v_cvt_pk_bf16_f32 v10, v10, s0
	ds_write_b16 v18, v10 offset:3600
	v_mul_f32_e32 v10, v43, v60
	v_cvt_pk_bf16_f32 v10, v10, s0
	ds_write_b16 v18, v10 offset:3744
	v_mul_f32_e32 v10, v44, v60
	v_cvt_pk_bf16_f32 v10, v10, s0
	ds_write_b16 v18, v10 offset:3888
	v_mul_f32_e32 v10, v46, v60
	v_cvt_pk_bf16_f32 v10, v10, s0
	v_cvt_pk_bf16_f32 v11, v11, s0
	ds_write_b16 v18, v10 offset:4032
	v_mul_f32_e32 v10, v47, v60
	v_cvt_pk_bf16_f32 v58, v14, v15
	v_cvt_pk_bf16_f32 v59, v16, v17
	ds_write_b16 v18, v11
	v_cvt_pk_bf16_f32 v19, v10, s0
	v_mfma_f32_32x32x16_bf16 v[2:17], v[6:9], v[2:5], 0
	ds_write_b16 v18, v19 offset:4176
	v_mul_f32_e32 v19, v48, v60
	v_cvt_pk_bf16_f32 v19, v19, s0
	ds_write_b16 v18, v19 offset:4320
	v_mul_f32_e32 v19, v49, v60
	v_cvt_pk_bf16_f32 v19, v19, s0
	ds_write_b16 v18, v19 offset:4464
	v_mfma_f32_32x32x16_bf16 v[2:17], v[52:55], v[56:59], v[2:17]
	v_mul_u32_u24_e32 v18, 0x240, v110
	v_add3_u32 v18, s72, v18, v50
	s_waitcnt lgkmcnt(14)
	s_nop 8
	v_mul_f32_e64 v2, v61, -v2
	v_cvt_pk_bf16_f32 v2, v2, s0
	ds_write_b16 v18, v2 offset:4608
	v_mul_f32_e64 v2, v61, -v3
	v_cvt_pk_bf16_f32 v2, v2, s0
	ds_write_b16 v18, v2 offset:4752
	v_mul_f32_e64 v2, v61, -v4
	v_cvt_pk_bf16_f32 v2, v2, s0
	ds_write_b16 v18, v2 offset:4896
	v_mul_f32_e64 v2, v61, -v5
	v_cvt_pk_bf16_f32 v2, v2, s0
	ds_write_b16 v18, v2 offset:5040
	v_mul_f32_e64 v2, v61, -v6
	v_cvt_pk_bf16_f32 v2, v2, s0
	ds_write_b16 v18, v2 offset:5760
	v_mul_f32_e64 v2, v61, -v7
	v_cvt_pk_bf16_f32 v2, v2, s0
	ds_write_b16 v18, v2 offset:5904
	v_mul_f32_e64 v2, v61, -v8
	v_cvt_pk_bf16_f32 v2, v2, s0
	ds_write_b16 v18, v2 offset:6048
	v_mul_f32_e64 v2, v61, -v9
	v_cvt_pk_bf16_f32 v2, v2, s0
	ds_write_b16 v18, v2 offset:6192
	v_mul_f32_e64 v2, v61, -v10
	v_cvt_pk_bf16_f32 v2, v2, s0
	ds_write_b16 v18, v2 offset:6912
	v_mul_f32_e64 v2, v61, -v11
	v_cvt_pk_bf16_f32 v2, v2, s0
	ds_write_b16 v18, v2 offset:7056
	v_mul_f32_e64 v2, v61, -v12
	v_cvt_pk_bf16_f32 v2, v2, s0
	ds_write_b16 v18, v2 offset:7200
	v_mul_f32_e64 v2, v61, -v13
	v_cvt_pk_bf16_f32 v2, v2, s0
	ds_write_b16 v18, v2 offset:7344
	v_mul_f32_e64 v2, v61, -v14
	v_cvt_pk_bf16_f32 v2, v2, s0
	ds_write_b16 v18, v2 offset:8064
	v_mul_f32_e64 v2, v61, -v15
	v_cvt_pk_bf16_f32 v2, v2, s0
	ds_write_b16 v18, v2 offset:8208
	v_mul_f32_e64 v2, v61, -v16
	v_cvt_pk_bf16_f32 v2, v2, s0
	ds_write_b16 v18, v2 offset:8352
	v_mul_f32_e64 v2, v61, -v17
	v_cvt_pk_bf16_f32 v2, v2, s0
	ds_write_b16 v18, v2 offset:8496

	.amdhsa_kernel _Z8mega_fwd4Args
		.amdhsa_group_segment_fixed_size 0
		.amdhsa_private_segment_fixed_size 0
		.amdhsa_kernarg_size 400
		.amdhsa_user_sgpr_count 2
		.amdhsa_user_sgpr_dispatch_ptr 0
		.amdhsa_user_sgpr_queue_ptr 0
		.amdhsa_user_sgpr_kernarg_segment_ptr 1
		.amdhsa_user_sgpr_dispatch_id 0
		.amdhsa_user_sgpr_kernarg_preload_length 0
		.amdhsa_user_sgpr_kernarg_preload_offset 0
		.amdhsa_user_sgpr_private_segment_size 0
		.amdhsa_uses_dynamic_stack 0
		.amdhsa_enable_private_segment 0
		.amdhsa_system_sgpr_workgroup_id_x 1
		.amdhsa_system_sgpr_workgroup_id_y 0
		.amdhsa_system_sgpr_workgroup_id_z 0
		.amdhsa_system_sgpr_workgroup_info 0
		.amdhsa_system_vgpr_workitem_id 0
		.amdhsa_next_free_vgpr 253
		.amdhsa_next_free_sgpr 100
		.amdhsa_accum_offset 256
		.amdhsa_reserve_vcc 1
		.amdhsa_float_round_mode_32 0
		.amdhsa_float_round_mode_16_64 0
		.amdhsa_float_denorm_mode_32 3
		.amdhsa_float_denorm_mode_16_64 3
		.amdhsa_dx10_clamp 1
		.amdhsa_ieee_mode 1
		.amdhsa_fp16_overflow 0
		.amdhsa_tg_split 0
		.amdhsa_exception_fp_ieee_invalid_op 0
		.amdhsa_exception_fp_denorm_src 0
		.amdhsa_exception_fp_ieee_div_zero 0
		.amdhsa_exception_fp_ieee_overflow 0
		.amdhsa_exception_fp_ieee_underflow 0
		.amdhsa_exception_fp_ieee_inexact 0
		.amdhsa_exception_int_div_zero 0
	.end_amdhsa_kernel

amdhsa.kernels:
  - .agpr_count:     0
    .args:
      - .offset:         0
        .size:           144
        .value_kind:     by_value
      - .offset:         144
        .size:           4
        .value_kind:     hidden_block_count_x
      - .offset:         148
        .size:           4
        .value_kind:     hidden_block_count_y
      - .offset:         152
        .size:           4
        .value_kind:     hidden_block_count_z
      - .offset:         156
        .size:           2
        .value_kind:     hidden_group_size_x
      - .offset:         158
        .size:           2
        .value_kind:     hidden_group_size_y
      - .offset:         160
        .size:           2
        .value_kind:     hidden_group_size_z
      - .offset:         162
        .size:           2
        .value_kind:     hidden_remainder_x
      - .offset:         164
        .size:           2
        .value_kind:     hidden_remainder_y
      - .offset:         166
        .size:           2
        .value_kind:     hidden_remainder_z
      - .offset:         184
        .size:           8
        .value_kind:     hidden_global_offset_x
      - .offset:         192
        .size:           8
        .value_kind:     hidden_global_offset_y
      - .offset:         200
        .size:           8
        .value_kind:     hidden_global_offset_z
      - .offset:         208
        .size:           2
        .value_kind:     hidden_grid_dims
      - .offset:         264
        .size:           4
        .value_kind:     hidden_dynamic_lds_size
    .group_segment_fixed_size: 0
    .kernarg_segment_align: 8
    .kernarg_segment_size: 400
    .language:       OpenCL C
    .language_version:
      - 2
      - 0
    .max_flat_workgroup_size: 512
    .name:           _Z8mega_fwd4Args
    .private_segment_fixed_size: 0
    .sgpr_count:     106
    .sgpr_spill_count: 43
    .symbol:         _Z8mega_fwd4Args.kd
    .uniform_work_group_size: 1
    .uses_dynamic_stack: false
    .vgpr_count:     253
    .vgpr_spill_count: 0
    .wavefront_size: 64
